# speedup vs baseline: 1.0326x; 1.0206x over previous
_Z11gemm_kernelILi1ELi1EEvPKDF16_S1_iiPKfS3_S3_PDF16_S4_S4_Pf:
	s_load_dwordx4 s[4:7], s[0:1], 0x0
	s_load_dwordx2 s[8:9], s[0:1], 0x48
	s_load_dwordx2 s[10:11], s[0:1], 0x18
	v_readfirstlane_b32 s12, v0
	v_and_b32_e32 v1, 63, v0
	s_lshr_b32 s12, s12, 6
	s_lshr_b32 s13, s12, 1
	s_and_b32 s14, s12, 1
	s_and_b32 s15, s2, 7
	s_lshr_b32 s16, s2, 3
	s_lshr_b32 s17, s16, 4
	s_lshl_b32 s15, s15, 2
	s_add_i32 s15, s15, s17
	s_and_b32 s16, s16, 15
	v_lshrrev_b32_e32 v2, 3, v1
	v_and_b32_e32 v3, 7, v1
	v_lshrrev_b32_e32 v4, 1, v2
	v_xor_b32_e32 v3, v3, v4
	v_lshlrev_b32_e32 v3, 4, v3
	v_lshl_or_b32 v2, v2, 11, v3
	v_xor_b32_e32 v3, 64, v2
	v_add_u32_e32 v3, 0x4000, v3
	v_add_u32_e32 v4, 0x8000, v2
	v_add_u32_e32 v5, 0x8000, v3
	v_and_b32_e32 v14, 31, v1
	v_lshrrev_b32_e32 v15, 5, v1
	v_bfe_u32 v16, v1, 1, 3
	v_xor_b32_e32 v16, v16, v15
	v_lshlrev_b32_e32 v16, 4, v16
	v_lshl_or_b32 v16, v14, 7, v16
	s_lshl_b32 s18, s13, 13
	s_lshl_b32 s19, s14, 12
	s_add_i32 s19, s19, 0xc000
	v_add_u32_e32 v6, s18, v16
	v_add_u32_e32 v10, s19, v16
	v_xor_b32_e32 v7, 0x20, v6
	v_xor_b32_e32 v11, 0x20, v10
	v_xor_b32_e32 v8, 0x40, v6
	v_xor_b32_e32 v12, 0x40, v10
	v_xor_b32_e32 v9, 0x60, v6
	v_xor_b32_e32 v13, 0x60, v10
	v_lshlrev_b32_e32 v15, 14, v15
	v_lshl_or_b32 v15, v14, 2, v15
	v_lshlrev_b32_e32 v14, 2, v14
	s_lshl_b32 s20, s12, 12
	s_lshl_b32 s21, s12, 11
	s_add_i32 s21, s21, 0xc000
	s_lshl_b32 s22, s16, 8
	s_lshl_b32 s23, s14, 7
	s_add_i32 s22, s22, s23
	s_waitcnt lgkmcnt(0)
	s_add_u32 s10, s10, s22
	s_addc_u32 s11, s11, 0
	global_load_dword v14, v14, s[10:11]
	s_lshl_b32 s23, s15, 18
	s_lshl_b32 s24, s12, 16
	s_add_i32 s23, s23, s24
	s_add_u32 s4, s4, s23
	s_addc_u32 s5, s5, 0
	s_lshl_b32 s23, s16, 17
	s_lshl_b32 s24, s12, 15
	s_add_i32 s23, s23, s24
	s_add_u32 s6, s6, s23
	s_addc_u32 s7, s7, 0
	s_lshl_b32 s23, s15, 19
	s_lshl_b32 s24, s13, 18
	s_add_i32 s23, s23, s24
	s_add_i32 s23, s23, s22
	s_add_u32 s8, s8, s23
	s_addc_u32 s9, s9, 0
	v_accvgpr_write_b32 a0, 0
	v_accvgpr_write_b32 a1, 0
	v_accvgpr_write_b32 a2, 0
	v_accvgpr_write_b32 a3, 0
	v_accvgpr_write_b32 a4, 0
	v_accvgpr_write_b32 a5, 0
	v_accvgpr_write_b32 a6, 0
	v_accvgpr_write_b32 a7, 0
	v_accvgpr_write_b32 a8, 0
	v_accvgpr_write_b32 a9, 0
	v_accvgpr_write_b32 a10, 0
	v_accvgpr_write_b32 a11, 0
	v_accvgpr_write_b32 a12, 0
	v_accvgpr_write_b32 a13, 0
	v_accvgpr_write_b32 a14, 0
	v_accvgpr_write_b32 a15, 0
	v_accvgpr_write_b32 a16, 0
	v_accvgpr_write_b32 a17, 0
	v_accvgpr_write_b32 a18, 0
	v_accvgpr_write_b32 a19, 0
	v_accvgpr_write_b32 a20, 0
	v_accvgpr_write_b32 a21, 0
	v_accvgpr_write_b32 a22, 0
	v_accvgpr_write_b32 a23, 0
	v_accvgpr_write_b32 a24, 0
	v_accvgpr_write_b32 a25, 0
	v_accvgpr_write_b32 a26, 0
	v_accvgpr_write_b32 a27, 0
	v_accvgpr_write_b32 a28, 0
	v_accvgpr_write_b32 a29, 0
	v_accvgpr_write_b32 a30, 0
	v_accvgpr_write_b32 a31, 0
	s_add_u32 m0, s20, 0x0
	s_nop 0
	global_load_lds_dwordx4 v2, s[4:5]
	s_add_u32 m0, s20, 0x400
	s_nop 0
	global_load_lds_dwordx4 v3, s[4:5]
	s_add_u32 m0, s20, 0x800
	s_nop 0
	global_load_lds_dwordx4 v4, s[4:5]
	s_add_u32 m0, s20, 0xc00
	s_nop 0
	global_load_lds_dwordx4 v5, s[4:5]
	s_add_u32 m0, s21, 0x0
	s_nop 0
	global_load_lds_dwordx4 v2, s[6:7]
	s_add_u32 m0, s21, 0x400
	s_nop 0
	global_load_lds_dwordx4 v3, s[6:7]
	s_add_u32 s4, s4, 0x80
	s_addc_u32 s5, s5, 0
	s_add_u32 s6, s6, 0x80
	s_addc_u32 s7, s7, 0
	s_add_u32 m0, s20, 0x4000
	s_nop 0
	global_load_lds_dwordx4 v2, s[4:5]
	s_add_u32 m0, s20, 0x4400
	s_nop 0
	global_load_lds_dwordx4 v3, s[4:5]
	s_add_u32 m0, s20, 0x4800
	s_nop 0
	global_load_lds_dwordx4 v4, s[4:5]
	s_add_u32 m0, s20, 0x4c00
	s_nop 0
	global_load_lds_dwordx4 v5, s[4:5]
	s_add_u32 m0, s21, 0x2000
	s_nop 0
	global_load_lds_dwordx4 v2, s[6:7]
	s_add_u32 m0, s21, 0x2400
	s_nop 0
	global_load_lds_dwordx4 v3, s[6:7]
	s_add_u32 s4, s4, 0x80
	s_addc_u32 s5, s5, 0
	s_add_u32 s6, s6, 0x80
	s_addc_u32 s7, s7, 0
	s_waitcnt vmcnt(6)
	s_barrier
	ds_read_b128 v[16:19], v6 offset:0
	ds_read_b128 v[20:23], v6 offset:4096
	ds_read_b128 v[24:27], v10 offset:0
	s_add_u32 m0, s20, 0x8000
	ds_read_b128 v[28:31], v7 offset:0
	global_load_lds_dwordx4 v2, s[4:5]
	s_add_u32 m0, s20, 0x8400
	ds_read_b128 v[32:35], v7 offset:4096
	global_load_lds_dwordx4 v3, s[4:5]
	s_add_u32 m0, s20, 0x8800
	ds_read_b128 v[36:39], v11 offset:0
	global_load_lds_dwordx4 v4, s[4:5]
	s_add_u32 m0, s20, 0x8c00
	ds_read_b128 v[40:43], v8 offset:0
	global_load_lds_dwordx4 v5, s[4:5]
	s_add_u32 m0, s21, 0x4000
	ds_read_b128 v[44:47], v8 offset:4096
	global_load_lds_dwordx4 v2, s[6:7]
	s_add_u32 m0, s21, 0x4400
	ds_read_b128 v[48:51], v12 offset:0
	global_load_lds_dwordx4 v3, s[6:7]
	ds_read_b128 v[52:55], v9 offset:0
	ds_read_b128 v[56:59], v9 offset:4096
	ds_read_b128 v[60:63], v13 offset:0
	s_add_u32 s4, s4, 0x80
	s_addc_u32 s5, s5, 0
	s_add_u32 s6, s6, 0x80
	s_addc_u32 s7, s7, 0
	s_waitcnt lgkmcnt(9)
	v_mfma_f32_32x32x16_f16 a[0:15], v[16:19], v[24:27], a[0:15]
	v_mfma_f32_32x32x16_f16 a[16:31], v[20:23], v[24:27], a[16:31]
	s_waitcnt lgkmcnt(6)
	v_mfma_f32_32x32x16_f16 a[0:15], v[28:31], v[36:39], a[0:15]
	v_mfma_f32_32x32x16_f16 a[16:31], v[32:35], v[36:39], a[16:31]
	s_waitcnt lgkmcnt(3)
	v_mfma_f32_32x32x16_f16 a[0:15], v[40:43], v[48:51], a[0:15]
	v_mfma_f32_32x32x16_f16 a[16:31], v[44:47], v[48:51], a[16:31]
	s_waitcnt lgkmcnt(0)
	v_mfma_f32_32x32x16_f16 a[0:15], v[52:55], v[60:63], a[0:15]
	v_mfma_f32_32x32x16_f16 a[16:31], v[56:59], v[60:63], a[16:31]
	s_waitcnt vmcnt(6)
	s_barrier
	ds_read_b128 v[16:19], v6 offset:16384
	ds_read_b128 v[20:23], v6 offset:20480
	ds_read_b128 v[24:27], v10 offset:8192
	s_add_u32 m0, s20, 0x0
	ds_read_b128 v[28:31], v7 offset:16384
	global_load_lds_dwordx4 v2, s[4:5]
	s_add_u32 m0, s20, 0x400
	ds_read_b128 v[32:35], v7 offset:20480
	global_load_lds_dwordx4 v3, s[4:5]
	s_add_u32 m0, s20, 0x800
	ds_read_b128 v[36:39], v11 offset:8192
	global_load_lds_dwordx4 v4, s[4:5]
	s_add_u32 m0, s20, 0xc00
	ds_read_b128 v[40:43], v8 offset:16384
	global_load_lds_dwordx4 v5, s[4:5]
	s_add_u32 m0, s21, 0x0
	ds_read_b128 v[44:47], v8 offset:20480
	global_load_lds_dwordx4 v2, s[6:7]
	s_add_u32 m0, s21, 0x400
	ds_read_b128 v[48:51], v12 offset:8192
	global_load_lds_dwordx4 v3, s[6:7]
	ds_read_b128 v[52:55], v9 offset:16384
	ds_read_b128 v[56:59], v9 offset:20480
	ds_read_b128 v[60:63], v13 offset:8192
	s_add_u32 s4, s4, 0x80
	s_addc_u32 s5, s5, 0
	s_add_u32 s6, s6, 0x80
	s_addc_u32 s7, s7, 0
	s_waitcnt lgkmcnt(9)
	v_mfma_f32_32x32x16_f16 a[0:15], v[16:19], v[24:27], a[0:15]
	v_mfma_f32_32x32x16_f16 a[16:31], v[20:23], v[24:27], a[16:31]
	s_waitcnt lgkmcnt(6)
	v_mfma_f32_32x32x16_f16 a[0:15], v[28:31], v[36:39], a[0:15]
	v_mfma_f32_32x32x16_f16 a[16:31], v[32:35], v[36:39], a[16:31]
	s_waitcnt lgkmcnt(3)
	v_mfma_f32_32x32x16_f16 a[0:15], v[40:43], v[48:51], a[0:15]
	v_mfma_f32_32x32x16_f16 a[16:31], v[44:47], v[48:51], a[16:31]
	s_waitcnt lgkmcnt(0)
	v_mfma_f32_32x32x16_f16 a[0:15], v[52:55], v[60:63], a[0:15]
	v_mfma_f32_32x32x16_f16 a[16:31], v[56:59], v[60:63], a[16:31]
	s_waitcnt vmcnt(6)
	s_barrier
	ds_read_b128 v[16:19], v6 offset:32768
	ds_read_b128 v[20:23], v6 offset:36864
	ds_read_b128 v[24:27], v10 offset:16384
	s_add_u32 m0, s20, 0x4000
	ds_read_b128 v[28:31], v7 offset:32768
	global_load_lds_dwordx4 v2, s[4:5]
	s_add_u32 m0, s20, 0x4400
	ds_read_b128 v[32:35], v7 offset:36864
	global_load_lds_dwordx4 v3, s[4:5]
	s_add_u32 m0, s20, 0x4800
	ds_read_b128 v[36:39], v11 offset:16384
	global_load_lds_dwordx4 v4, s[4:5]
	s_add_u32 m0, s20, 0x4c00
	ds_read_b128 v[40:43], v8 offset:32768
	global_load_lds_dwordx4 v5, s[4:5]
	s_add_u32 m0, s21, 0x2000
	ds_read_b128 v[44:47], v8 offset:36864
	global_load_lds_dwordx4 v2, s[6:7]
	s_add_u32 m0, s21, 0x2400
	ds_read_b128 v[48:51], v12 offset:16384
	global_load_lds_dwordx4 v3, s[6:7]
	ds_read_b128 v[52:55], v9 offset:32768
	ds_read_b128 v[56:59], v9 offset:36864
	ds_read_b128 v[60:63], v13 offset:16384
	s_add_u32 s4, s4, 0x80
	s_addc_u32 s5, s5, 0
	s_add_u32 s6, s6, 0x80
	s_addc_u32 s7, s7, 0
	s_waitcnt lgkmcnt(9)
	v_mfma_f32_32x32x16_f16 a[0:15], v[16:19], v[24:27], a[0:15]
	v_mfma_f32_32x32x16_f16 a[16:31], v[20:23], v[24:27], a[16:31]
	s_waitcnt lgkmcnt(6)
	v_mfma_f32_32x32x16_f16 a[0:15], v[28:31], v[36:39], a[0:15]
	v_mfma_f32_32x32x16_f16 a[16:31], v[32:35], v[36:39], a[16:31]
	s_waitcnt lgkmcnt(3)
	v_mfma_f32_32x32x16_f16 a[0:15], v[40:43], v[48:51], a[0:15]
	v_mfma_f32_32x32x16_f16 a[16:31], v[44:47], v[48:51], a[16:31]
	s_waitcnt lgkmcnt(0)
	v_mfma_f32_32x32x16_f16 a[0:15], v[52:55], v[60:63], a[0:15]
	v_mfma_f32_32x32x16_f16 a[16:31], v[56:59], v[60:63], a[16:31]
	s_waitcnt vmcnt(6)
	s_barrier
	ds_read_b128 v[16:19], v6 offset:0
	ds_read_b128 v[20:23], v6 offset:4096
	ds_read_b128 v[24:27], v10 offset:0
	s_add_u32 m0, s20, 0x8000
	ds_read_b128 v[28:31], v7 offset:0
	global_load_lds_dwordx4 v2, s[4:5]
	s_add_u32 m0, s20, 0x8400
	ds_read_b128 v[32:35], v7 offset:4096
	global_load_lds_dwordx4 v3, s[4:5]
	s_add_u32 m0, s20, 0x8800
	ds_read_b128 v[36:39], v11 offset:0
	global_load_lds_dwordx4 v4, s[4:5]
	s_add_u32 m0, s20, 0x8c00
	ds_read_b128 v[40:43], v8 offset:0
	global_load_lds_dwordx4 v5, s[4:5]
	s_add_u32 m0, s21, 0x4000
	ds_read_b128 v[44:47], v8 offset:4096
	global_load_lds_dwordx4 v2, s[6:7]
	s_add_u32 m0, s21, 0x4400
	ds_read_b128 v[48:51], v12 offset:0
	global_load_lds_dwordx4 v3, s[6:7]
	ds_read_b128 v[52:55], v9 offset:0
	ds_read_b128 v[56:59], v9 offset:4096
	ds_read_b128 v[60:63], v13 offset:0
	s_add_u32 s4, s4, 0x80
	s_addc_u32 s5, s5, 0
	s_add_u32 s6, s6, 0x80
	s_addc_u32 s7, s7, 0
	s_waitcnt lgkmcnt(9)
	v_mfma_f32_32x32x16_f16 a[0:15], v[16:19], v[24:27], a[0:15]
	v_mfma_f32_32x32x16_f16 a[16:31], v[20:23], v[24:27], a[16:31]
	s_waitcnt lgkmcnt(6)
	v_mfma_f32_32x32x16_f16 a[0:15], v[28:31], v[36:39], a[0:15]
	v_mfma_f32_32x32x16_f16 a[16:31], v[32:35], v[36:39], a[16:31]
	s_waitcnt lgkmcnt(3)
	v_mfma_f32_32x32x16_f16 a[0:15], v[40:43], v[48:51], a[0:15]
	v_mfma_f32_32x32x16_f16 a[16:31], v[44:47], v[48:51], a[16:31]
	s_waitcnt lgkmcnt(0)
	v_mfma_f32_32x32x16_f16 a[0:15], v[52:55], v[60:63], a[0:15]
	v_mfma_f32_32x32x16_f16 a[16:31], v[56:59], v[60:63], a[16:31]
	s_waitcnt vmcnt(6)
	s_barrier
	ds_read_b128 v[16:19], v6 offset:16384
	ds_read_b128 v[20:23], v6 offset:20480
	ds_read_b128 v[24:27], v10 offset:8192
	s_add_u32 m0, s20, 0x0
	ds_read_b128 v[28:31], v7 offset:16384
	global_load_lds_dwordx4 v2, s[4:5]
	s_add_u32 m0, s20, 0x400
	ds_read_b128 v[32:35], v7 offset:20480
	global_load_lds_dwordx4 v3, s[4:5]
	s_add_u32 m0, s20, 0x800
	ds_read_b128 v[36:39], v11 offset:8192
	global_load_lds_dwordx4 v4, s[4:5]
	s_add_u32 m0, s20, 0xc00
	ds_read_b128 v[40:43], v8 offset:16384
	global_load_lds_dwordx4 v5, s[4:5]
	s_add_u32 m0, s21, 0x0
	ds_read_b128 v[44:47], v8 offset:20480
	global_load_lds_dwordx4 v2, s[6:7]
	s_add_u32 m0, s21, 0x400
	ds_read_b128 v[48:51], v12 offset:8192
	global_load_lds_dwordx4 v3, s[6:7]
	ds_read_b128 v[52:55], v9 offset:16384
	ds_read_b128 v[56:59], v9 offset:20480
	ds_read_b128 v[60:63], v13 offset:8192
	s_add_u32 s4, s4, 0x80
	s_addc_u32 s5, s5, 0
	s_add_u32 s6, s6, 0x80
	s_addc_u32 s7, s7, 0
	s_waitcnt lgkmcnt(9)
	v_mfma_f32_32x32x16_f16 a[0:15], v[16:19], v[24:27], a[0:15]
	v_mfma_f32_32x32x16_f16 a[16:31], v[20:23], v[24:27], a[16:31]
	s_waitcnt lgkmcnt(6)
	v_mfma_f32_32x32x16_f16 a[0:15], v[28:31], v[36:39], a[0:15]
	v_mfma_f32_32x32x16_f16 a[16:31], v[32:35], v[36:39], a[16:31]
	s_waitcnt lgkmcnt(3)
	v_mfma_f32_32x32x16_f16 a[0:15], v[40:43], v[48:51], a[0:15]
	v_mfma_f32_32x32x16_f16 a[16:31], v[44:47], v[48:51], a[16:31]
	s_waitcnt lgkmcnt(0)
	v_mfma_f32_32x32x16_f16 a[0:15], v[52:55], v[60:63], a[0:15]
	v_mfma_f32_32x32x16_f16 a[16:31], v[56:59], v[60:63], a[16:31]
	s_waitcnt vmcnt(6)
	s_barrier
	ds_read_b128 v[16:19], v6 offset:32768
	ds_read_b128 v[20:23], v6 offset:36864
	ds_read_b128 v[24:27], v10 offset:16384
	s_add_u32 m0, s20, 0x4000
	ds_read_b128 v[28:31], v7 offset:32768
	global_load_lds_dwordx4 v2, s[4:5]
	s_add_u32 m0, s20, 0x4400
	ds_read_b128 v[32:35], v7 offset:36864
	global_load_lds_dwordx4 v3, s[4:5]
	s_add_u32 m0, s20, 0x4800
	ds_read_b128 v[36:39], v11 offset:16384
	global_load_lds_dwordx4 v4, s[4:5]
	s_add_u32 m0, s20, 0x4c00
	ds_read_b128 v[40:43], v8 offset:32768
	global_load_lds_dwordx4 v5, s[4:5]
	s_add_u32 m0, s21, 0x2000
	ds_read_b128 v[44:47], v8 offset:36864
	global_load_lds_dwordx4 v2, s[6:7]
	s_add_u32 m0, s21, 0x2400
	ds_read_b128 v[48:51], v12 offset:16384
	global_load_lds_dwordx4 v3, s[6:7]
	ds_read_b128 v[52:55], v9 offset:32768
	ds_read_b128 v[56:59], v9 offset:36864
	ds_read_b128 v[60:63], v13 offset:16384
	s_add_u32 s4, s4, 0x80
	s_addc_u32 s5, s5, 0
	s_add_u32 s6, s6, 0x80
	s_addc_u32 s7, s7, 0
	s_waitcnt lgkmcnt(9)
	v_mfma_f32_32x32x16_f16 a[0:15], v[16:19], v[24:27], a[0:15]
	v_mfma_f32_32x32x16_f16 a[16:31], v[20:23], v[24:27], a[16:31]
	s_waitcnt lgkmcnt(6)
	v_mfma_f32_32x32x16_f16 a[0:15], v[28:31], v[36:39], a[0:15]
	v_mfma_f32_32x32x16_f16 a[16:31], v[32:35], v[36:39], a[16:31]
	s_waitcnt lgkmcnt(3)
	v_mfma_f32_32x32x16_f16 a[0:15], v[40:43], v[48:51], a[0:15]
	v_mfma_f32_32x32x16_f16 a[16:31], v[44:47], v[48:51], a[16:31]
	s_waitcnt lgkmcnt(0)
	v_mfma_f32_32x32x16_f16 a[0:15], v[52:55], v[60:63], a[0:15]
	v_mfma_f32_32x32x16_f16 a[16:31], v[56:59], v[60:63], a[16:31]
	s_waitcnt vmcnt(6)
	s_barrier
	ds_read_b128 v[16:19], v6 offset:0
	ds_read_b128 v[20:23], v6 offset:4096
	ds_read_b128 v[24:27], v10 offset:0
	s_add_u32 m0, s20, 0x8000
	ds_read_b128 v[28:31], v7 offset:0
	global_load_lds_dwordx4 v2, s[4:5]
	s_add_u32 m0, s20, 0x8400
	ds_read_b128 v[32:35], v7 offset:4096
	global_load_lds_dwordx4 v3, s[4:5]
	s_add_u32 m0, s20, 0x8800
	ds_read_b128 v[36:39], v11 offset:0
	global_load_lds_dwordx4 v4, s[4:5]
	s_add_u32 m0, s20, 0x8c00
	ds_read_b128 v[40:43], v8 offset:0
	global_load_lds_dwordx4 v5, s[4:5]
	s_add_u32 m0, s21, 0x4000
	ds_read_b128 v[44:47], v8 offset:4096
	global_load_lds_dwordx4 v2, s[6:7]
	s_add_u32 m0, s21, 0x4400
	ds_read_b128 v[48:51], v12 offset:0
	global_load_lds_dwordx4 v3, s[6:7]
	ds_read_b128 v[52:55], v9 offset:0
	ds_read_b128 v[56:59], v9 offset:4096
	ds_read_b128 v[60:63], v13 offset:0
	s_add_u32 s4, s4, 0x80
	s_addc_u32 s5, s5, 0
	s_add_u32 s6, s6, 0x80
	s_addc_u32 s7, s7, 0
	s_waitcnt lgkmcnt(9)
	v_mfma_f32_32x32x16_f16 a[0:15], v[16:19], v[24:27], a[0:15]
	v_mfma_f32_32x32x16_f16 a[16:31], v[20:23], v[24:27], a[16:31]
	s_waitcnt lgkmcnt(6)
	v_mfma_f32_32x32x16_f16 a[0:15], v[28:31], v[36:39], a[0:15]
	v_mfma_f32_32x32x16_f16 a[16:31], v[32:35], v[36:39], a[16:31]
	s_waitcnt lgkmcnt(3)
	v_mfma_f32_32x32x16_f16 a[0:15], v[40:43], v[48:51], a[0:15]
	v_mfma_f32_32x32x16_f16 a[16:31], v[44:47], v[48:51], a[16:31]
	s_waitcnt lgkmcnt(0)
	v_mfma_f32_32x32x16_f16 a[0:15], v[52:55], v[60:63], a[0:15]
	v_mfma_f32_32x32x16_f16 a[16:31], v[56:59], v[60:63], a[16:31]
	s_waitcnt vmcnt(6)
	s_barrier
	ds_read_b128 v[16:19], v6 offset:16384
	ds_read_b128 v[20:23], v6 offset:20480
	ds_read_b128 v[24:27], v10 offset:8192
	s_add_u32 m0, s20, 0x0
	ds_read_b128 v[28:31], v7 offset:16384
	global_load_lds_dwordx4 v2, s[4:5]
	s_add_u32 m0, s20, 0x400
	ds_read_b128 v[32:35], v7 offset:20480
	global_load_lds_dwordx4 v3, s[4:5]
	s_add_u32 m0, s20, 0x800
	ds_read_b128 v[36:39], v11 offset:8192
	global_load_lds_dwordx4 v4, s[4:5]
	s_add_u32 m0, s20, 0xc00
	ds_read_b128 v[40:43], v8 offset:16384
	global_load_lds_dwordx4 v5, s[4:5]
	s_add_u32 m0, s21, 0x0
	ds_read_b128 v[44:47], v8 offset:20480
	global_load_lds_dwordx4 v2, s[6:7]
	s_add_u32 m0, s21, 0x400
	ds_read_b128 v[48:51], v12 offset:8192
	global_load_lds_dwordx4 v3, s[6:7]
	ds_read_b128 v[52:55], v9 offset:16384
	ds_read_b128 v[56:59], v9 offset:20480
	ds_read_b128 v[60:63], v13 offset:8192
	s_add_u32 s4, s4, 0x80
	s_addc_u32 s5, s5, 0
	s_add_u32 s6, s6, 0x80
	s_addc_u32 s7, s7, 0
	s_waitcnt lgkmcnt(9)
	v_mfma_f32_32x32x16_f16 a[0:15], v[16:19], v[24:27], a[0:15]
	v_mfma_f32_32x32x16_f16 a[16:31], v[20:23], v[24:27], a[16:31]
	s_waitcnt lgkmcnt(6)
	v_mfma_f32_32x32x16_f16 a[0:15], v[28:31], v[36:39], a[0:15]
	v_mfma_f32_32x32x16_f16 a[16:31], v[32:35], v[36:39], a[16:31]
	s_waitcnt lgkmcnt(3)
	v_mfma_f32_32x32x16_f16 a[0:15], v[40:43], v[48:51], a[0:15]
	v_mfma_f32_32x32x16_f16 a[16:31], v[44:47], v[48:51], a[16:31]
	s_waitcnt lgkmcnt(0)
	v_mfma_f32_32x32x16_f16 a[0:15], v[52:55], v[60:63], a[0:15]
	v_mfma_f32_32x32x16_f16 a[16:31], v[56:59], v[60:63], a[16:31]
	s_waitcnt vmcnt(6)
	s_barrier
	ds_read_b128 v[16:19], v6 offset:32768
	ds_read_b128 v[20:23], v6 offset:36864
	ds_read_b128 v[24:27], v10 offset:16384
	s_add_u32 m0, s20, 0x4000
	ds_read_b128 v[28:31], v7 offset:32768
	global_load_lds_dwordx4 v2, s[4:5]
	s_add_u32 m0, s20, 0x4400
	ds_read_b128 v[32:35], v7 offset:36864
	global_load_lds_dwordx4 v3, s[4:5]
	s_add_u32 m0, s20, 0x4800
	ds_read_b128 v[36:39], v11 offset:16384
	global_load_lds_dwordx4 v4, s[4:5]
	s_add_u32 m0, s20, 0x4c00
	ds_read_b128 v[40:43], v8 offset:32768
	global_load_lds_dwordx4 v5, s[4:5]
	s_add_u32 m0, s21, 0x2000
	ds_read_b128 v[44:47], v8 offset:36864
	global_load_lds_dwordx4 v2, s[6:7]
	s_add_u32 m0, s21, 0x2400
	ds_read_b128 v[48:51], v12 offset:16384
	global_load_lds_dwordx4 v3, s[6:7]
	ds_read_b128 v[52:55], v9 offset:32768
	ds_read_b128 v[56:59], v9 offset:36864
	ds_read_b128 v[60:63], v13 offset:16384
	s_add_u32 s4, s4, 0x80
	s_addc_u32 s5, s5, 0
	s_add_u32 s6, s6, 0x80
	s_addc_u32 s7, s7, 0
	s_waitcnt lgkmcnt(9)
	v_mfma_f32_32x32x16_f16 a[0:15], v[16:19], v[24:27], a[0:15]
	v_mfma_f32_32x32x16_f16 a[16:31], v[20:23], v[24:27], a[16:31]
	s_waitcnt lgkmcnt(6)
	v_mfma_f32_32x32x16_f16 a[0:15], v[28:31], v[36:39], a[0:15]
	v_mfma_f32_32x32x16_f16 a[16:31], v[32:35], v[36:39], a[16:31]
	s_waitcnt lgkmcnt(3)
	v_mfma_f32_32x32x16_f16 a[0:15], v[40:43], v[48:51], a[0:15]
	v_mfma_f32_32x32x16_f16 a[16:31], v[44:47], v[48:51], a[16:31]
	s_waitcnt lgkmcnt(0)
	v_mfma_f32_32x32x16_f16 a[0:15], v[52:55], v[60:63], a[0:15]
	v_mfma_f32_32x32x16_f16 a[16:31], v[56:59], v[60:63], a[16:31]
	s_waitcnt vmcnt(6)
	s_barrier
	ds_read_b128 v[16:19], v6 offset:0
	ds_read_b128 v[20:23], v6 offset:4096
	ds_read_b128 v[24:27], v10 offset:0
	s_add_u32 m0, s20, 0x8000
	ds_read_b128 v[28:31], v7 offset:0
	global_load_lds_dwordx4 v2, s[4:5]
	s_add_u32 m0, s20, 0x8400
	ds_read_b128 v[32:35], v7 offset:4096
	global_load_lds_dwordx4 v3, s[4:5]
	s_add_u32 m0, s20, 0x8800
	ds_read_b128 v[36:39], v11 offset:0
	global_load_lds_dwordx4 v4, s[4:5]
	s_add_u32 m0, s20, 0x8c00
	ds_read_b128 v[40:43], v8 offset:0
	global_load_lds_dwordx4 v5, s[4:5]
	s_add_u32 m0, s21, 0x4000
	ds_read_b128 v[44:47], v8 offset:4096
	global_load_lds_dwordx4 v2, s[6:7]
	s_add_u32 m0, s21, 0x4400
	ds_read_b128 v[48:51], v12 offset:0
	global_load_lds_dwordx4 v3, s[6:7]
	ds_read_b128 v[52:55], v9 offset:0
	ds_read_b128 v[56:59], v9 offset:4096
	ds_read_b128 v[60:63], v13 offset:0
	s_add_u32 s4, s4, 0x80
	s_addc_u32 s5, s5, 0
	s_add_u32 s6, s6, 0x80
	s_addc_u32 s7, s7, 0
	s_waitcnt lgkmcnt(9)
	v_mfma_f32_32x32x16_f16 a[0:15], v[16:19], v[24:27], a[0:15]
	v_mfma_f32_32x32x16_f16 a[16:31], v[20:23], v[24:27], a[16:31]
	s_waitcnt lgkmcnt(6)
	v_mfma_f32_32x32x16_f16 a[0:15], v[28:31], v[36:39], a[0:15]
	v_mfma_f32_32x32x16_f16 a[16:31], v[32:35], v[36:39], a[16:31]
	s_waitcnt lgkmcnt(3)
	v_mfma_f32_32x32x16_f16 a[0:15], v[40:43], v[48:51], a[0:15]
	v_mfma_f32_32x32x16_f16 a[16:31], v[44:47], v[48:51], a[16:31]
	s_waitcnt lgkmcnt(0)
	v_mfma_f32_32x32x16_f16 a[0:15], v[52:55], v[60:63], a[0:15]
	v_mfma_f32_32x32x16_f16 a[16:31], v[56:59], v[60:63], a[16:31]
	s_waitcnt vmcnt(6)
	s_barrier
	ds_read_b128 v[16:19], v6 offset:16384
	ds_read_b128 v[20:23], v6 offset:20480
	ds_read_b128 v[24:27], v10 offset:8192
	s_add_u32 m0, s20, 0x0
	ds_read_b128 v[28:31], v7 offset:16384
	global_load_lds_dwordx4 v2, s[4:5]
	s_add_u32 m0, s20, 0x400
	ds_read_b128 v[32:35], v7 offset:20480
	global_load_lds_dwordx4 v3, s[4:5]
	s_add_u32 m0, s20, 0x800
	ds_read_b128 v[36:39], v11 offset:8192
	global_load_lds_dwordx4 v4, s[4:5]
	s_add_u32 m0, s20, 0xc00
	ds_read_b128 v[40:43], v8 offset:16384
	global_load_lds_dwordx4 v5, s[4:5]
	s_add_u32 m0, s21, 0x0
	ds_read_b128 v[44:47], v8 offset:20480
	global_load_lds_dwordx4 v2, s[6:7]
	s_add_u32 m0, s21, 0x400
	ds_read_b128 v[48:51], v12 offset:8192
	global_load_lds_dwordx4 v3, s[6:7]
	ds_read_b128 v[52:55], v9 offset:16384
	ds_read_b128 v[56:59], v9 offset:20480
	ds_read_b128 v[60:63], v13 offset:8192
	s_add_u32 s4, s4, 0x80
	s_addc_u32 s5, s5, 0
	s_add_u32 s6, s6, 0x80
	s_addc_u32 s7, s7, 0
	s_waitcnt lgkmcnt(9)
	v_mfma_f32_32x32x16_f16 a[0:15], v[16:19], v[24:27], a[0:15]
	v_mfma_f32_32x32x16_f16 a[16:31], v[20:23], v[24:27], a[16:31]
	s_waitcnt lgkmcnt(6)
	v_mfma_f32_32x32x16_f16 a[0:15], v[28:31], v[36:39], a[0:15]
	v_mfma_f32_32x32x16_f16 a[16:31], v[32:35], v[36:39], a[16:31]
	s_waitcnt lgkmcnt(3)
	v_mfma_f32_32x32x16_f16 a[0:15], v[40:43], v[48:51], a[0:15]
	v_mfma_f32_32x32x16_f16 a[16:31], v[44:47], v[48:51], a[16:31]
	s_waitcnt lgkmcnt(0)
	v_mfma_f32_32x32x16_f16 a[0:15], v[52:55], v[60:63], a[0:15]
	v_mfma_f32_32x32x16_f16 a[16:31], v[56:59], v[60:63], a[16:31]
	s_waitcnt vmcnt(6)
	s_barrier
	ds_read_b128 v[16:19], v6 offset:32768
	ds_read_b128 v[20:23], v6 offset:36864
	ds_read_b128 v[24:27], v10 offset:16384
	s_add_u32 m0, s20, 0x4000
	ds_read_b128 v[28:31], v7 offset:32768
	global_load_lds_dwordx4 v2, s[4:5]
	s_add_u32 m0, s20, 0x4400
	ds_read_b128 v[32:35], v7 offset:36864
	global_load_lds_dwordx4 v3, s[4:5]
	s_add_u32 m0, s20, 0x4800
	ds_read_b128 v[36:39], v11 offset:16384
	global_load_lds_dwordx4 v4, s[4:5]
	s_add_u32 m0, s20, 0x4c00
	ds_read_b128 v[40:43], v8 offset:32768
	global_load_lds_dwordx4 v5, s[4:5]
	s_add_u32 m0, s21, 0x2000
	ds_read_b128 v[44:47], v8 offset:36864
	global_load_lds_dwordx4 v2, s[6:7]
	s_add_u32 m0, s21, 0x2400
	ds_read_b128 v[48:51], v12 offset:16384
	global_load_lds_dwordx4 v3, s[6:7]
	ds_read_b128 v[52:55], v9 offset:32768
	ds_read_b128 v[56:59], v9 offset:36864
	ds_read_b128 v[60:63], v13 offset:16384
	s_add_u32 s4, s4, 0x80
	s_addc_u32 s5, s5, 0
	s_add_u32 s6, s6, 0x80
	s_addc_u32 s7, s7, 0
	s_waitcnt lgkmcnt(9)
	v_mfma_f32_32x32x16_f16 a[0:15], v[16:19], v[24:27], a[0:15]
	v_mfma_f32_32x32x16_f16 a[16:31], v[20:23], v[24:27], a[16:31]
	s_waitcnt lgkmcnt(6)
	v_mfma_f32_32x32x16_f16 a[0:15], v[28:31], v[36:39], a[0:15]
	v_mfma_f32_32x32x16_f16 a[16:31], v[32:35], v[36:39], a[16:31]
	s_waitcnt lgkmcnt(3)
	v_mfma_f32_32x32x16_f16 a[0:15], v[40:43], v[48:51], a[0:15]
	v_mfma_f32_32x32x16_f16 a[16:31], v[44:47], v[48:51], a[16:31]
	s_waitcnt lgkmcnt(0)
	v_mfma_f32_32x32x16_f16 a[0:15], v[52:55], v[60:63], a[0:15]
	v_mfma_f32_32x32x16_f16 a[16:31], v[56:59], v[60:63], a[16:31]
	s_waitcnt vmcnt(6)
	s_barrier
	ds_read_b128 v[16:19], v6 offset:0
	ds_read_b128 v[20:23], v6 offset:4096
	ds_read_b128 v[24:27], v10 offset:0
	s_add_u32 m0, s20, 0x8000
	ds_read_b128 v[28:31], v7 offset:0
	global_load_lds_dwordx4 v2, s[4:5]
	s_add_u32 m0, s20, 0x8400
	ds_read_b128 v[32:35], v7 offset:4096
	global_load_lds_dwordx4 v3, s[4:5]
	s_add_u32 m0, s20, 0x8800
	ds_read_b128 v[36:39], v11 offset:0
	global_load_lds_dwordx4 v4, s[4:5]
	s_add_u32 m0, s20, 0x8c00
	ds_read_b128 v[40:43], v8 offset:0
	global_load_lds_dwordx4 v5, s[4:5]
	s_add_u32 m0, s21, 0x4000
	ds_read_b128 v[44:47], v8 offset:4096
	global_load_lds_dwordx4 v2, s[6:7]
	s_add_u32 m0, s21, 0x4400
	ds_read_b128 v[48:51], v12 offset:0
	global_load_lds_dwordx4 v3, s[6:7]
	ds_read_b128 v[52:55], v9 offset:0
	ds_read_b128 v[56:59], v9 offset:4096
	ds_read_b128 v[60:63], v13 offset:0
	s_add_u32 s4, s4, 0x80
	s_addc_u32 s5, s5, 0
	s_add_u32 s6, s6, 0x80
	s_addc_u32 s7, s7, 0
	s_waitcnt lgkmcnt(9)
	v_mfma_f32_32x32x16_f16 a[0:15], v[16:19], v[24:27], a[0:15]
	v_mfma_f32_32x32x16_f16 a[16:31], v[20:23], v[24:27], a[16:31]
	s_waitcnt lgkmcnt(6)
	v_mfma_f32_32x32x16_f16 a[0:15], v[28:31], v[36:39], a[0:15]
	v_mfma_f32_32x32x16_f16 a[16:31], v[32:35], v[36:39], a[16:31]
	s_waitcnt lgkmcnt(3)
	v_mfma_f32_32x32x16_f16 a[0:15], v[40:43], v[48:51], a[0:15]
	v_mfma_f32_32x32x16_f16 a[16:31], v[44:47], v[48:51], a[16:31]
	s_waitcnt lgkmcnt(0)
	v_mfma_f32_32x32x16_f16 a[0:15], v[52:55], v[60:63], a[0:15]
	v_mfma_f32_32x32x16_f16 a[16:31], v[56:59], v[60:63], a[16:31]
	s_waitcnt vmcnt(6)
	s_barrier
	ds_read_b128 v[16:19], v6 offset:16384
	ds_read_b128 v[20:23], v6 offset:20480
	ds_read_b128 v[24:27], v10 offset:8192
	s_add_u32 m0, s20, 0x0
	ds_read_b128 v[28:31], v7 offset:16384
	global_load_lds_dwordx4 v2, s[4:5]
	s_add_u32 m0, s20, 0x400
	ds_read_b128 v[32:35], v7 offset:20480
	global_load_lds_dwordx4 v3, s[4:5]
	s_add_u32 m0, s20, 0x800
	ds_read_b128 v[36:39], v11 offset:8192
	global_load_lds_dwordx4 v4, s[4:5]
	s_add_u32 m0, s20, 0xc00
	ds_read_b128 v[40:43], v8 offset:16384
	global_load_lds_dwordx4 v5, s[4:5]
	s_add_u32 m0, s21, 0x0
	ds_read_b128 v[44:47], v8 offset:20480
	global_load_lds_dwordx4 v2, s[6:7]
	s_add_u32 m0, s21, 0x400
	ds_read_b128 v[48:51], v12 offset:8192
	global_load_lds_dwordx4 v3, s[6:7]
	ds_read_b128 v[52:55], v9 offset:16384
	ds_read_b128 v[56:59], v9 offset:20480
	ds_read_b128 v[60:63], v13 offset:8192
	s_add_u32 s4, s4, 0x80
	s_addc_u32 s5, s5, 0
	s_add_u32 s6, s6, 0x80
	s_addc_u32 s7, s7, 0
	s_waitcnt lgkmcnt(9)
	v_mfma_f32_32x32x16_f16 a[0:15], v[16:19], v[24:27], a[0:15]
	v_mfma_f32_32x32x16_f16 a[16:31], v[20:23], v[24:27], a[16:31]
	s_waitcnt lgkmcnt(6)
	v_mfma_f32_32x32x16_f16 a[0:15], v[28:31], v[36:39], a[0:15]
	v_mfma_f32_32x32x16_f16 a[16:31], v[32:35], v[36:39], a[16:31]
	s_waitcnt lgkmcnt(3)
	v_mfma_f32_32x32x16_f16 a[0:15], v[40:43], v[48:51], a[0:15]
	v_mfma_f32_32x32x16_f16 a[16:31], v[44:47], v[48:51], a[16:31]
	s_waitcnt lgkmcnt(0)
	v_mfma_f32_32x32x16_f16 a[0:15], v[52:55], v[60:63], a[0:15]
	v_mfma_f32_32x32x16_f16 a[16:31], v[56:59], v[60:63], a[16:31]
	s_waitcnt vmcnt(6)
	s_barrier
	ds_read_b128 v[16:19], v6 offset:32768
	ds_read_b128 v[20:23], v6 offset:36864
	ds_read_b128 v[24:27], v10 offset:16384
	ds_read_b128 v[28:31], v7 offset:32768
	ds_read_b128 v[32:35], v7 offset:36864
	ds_read_b128 v[36:39], v11 offset:16384
	ds_read_b128 v[40:43], v8 offset:32768
	ds_read_b128 v[44:47], v8 offset:36864
	ds_read_b128 v[48:51], v12 offset:16384
	ds_read_b128 v[52:55], v9 offset:32768
	ds_read_b128 v[56:59], v9 offset:36864
	ds_read_b128 v[60:63], v13 offset:16384
	s_waitcnt lgkmcnt(9)
	v_mfma_f32_32x32x16_f16 a[0:15], v[16:19], v[24:27], a[0:15]
	v_mfma_f32_32x32x16_f16 a[16:31], v[20:23], v[24:27], a[16:31]
	s_waitcnt lgkmcnt(6)
	v_mfma_f32_32x32x16_f16 a[0:15], v[28:31], v[36:39], a[0:15]
	v_mfma_f32_32x32x16_f16 a[16:31], v[32:35], v[36:39], a[16:31]
	s_waitcnt lgkmcnt(3)
	v_mfma_f32_32x32x16_f16 a[0:15], v[40:43], v[48:51], a[0:15]
	v_mfma_f32_32x32x16_f16 a[16:31], v[44:47], v[48:51], a[16:31]
	s_waitcnt lgkmcnt(0)
	v_mfma_f32_32x32x16_f16 a[0:15], v[52:55], v[60:63], a[0:15]
	v_mfma_f32_32x32x16_f16 a[16:31], v[56:59], v[60:63], a[16:31]
	s_waitcnt vmcnt(0)
	s_barrier
	ds_read_b128 v[16:19], v6 offset:0
	ds_read_b128 v[20:23], v6 offset:4096
	ds_read_b128 v[24:27], v10 offset:0
	ds_read_b128 v[28:31], v7 offset:0
	ds_read_b128 v[32:35], v7 offset:4096
	ds_read_b128 v[36:39], v11 offset:0
	ds_read_b128 v[40:43], v8 offset:0
	ds_read_b128 v[44:47], v8 offset:4096
	ds_read_b128 v[48:51], v12 offset:0
	ds_read_b128 v[52:55], v9 offset:0
	ds_read_b128 v[56:59], v9 offset:4096
	ds_read_b128 v[60:63], v13 offset:0
	s_waitcnt lgkmcnt(9)
	v_mfma_f32_32x32x16_f16 a[0:15], v[16:19], v[24:27], a[0:15]
	v_mfma_f32_32x32x16_f16 a[16:31], v[20:23], v[24:27], a[16:31]
	s_waitcnt lgkmcnt(6)
	v_mfma_f32_32x32x16_f16 a[0:15], v[28:31], v[36:39], a[0:15]
	v_mfma_f32_32x32x16_f16 a[16:31], v[32:35], v[36:39], a[16:31]
	s_waitcnt lgkmcnt(3)
	v_mfma_f32_32x32x16_f16 a[0:15], v[40:43], v[48:51], a[0:15]
	v_mfma_f32_32x32x16_f16 a[16:31], v[44:47], v[48:51], a[16:31]
	s_waitcnt lgkmcnt(0)
	v_mfma_f32_32x32x16_f16 a[0:15], v[52:55], v[60:63], a[0:15]
	v_mfma_f32_32x32x16_f16 a[16:31], v[56:59], v[60:63], a[16:31]
	s_nop 15
	s_nop 3
	v_accvgpr_read_b32 v16, a0
	v_accvgpr_read_b32 v17, a1
	v_accvgpr_read_b32 v18, a2
	v_accvgpr_read_b32 v19, a3
	v_accvgpr_read_b32 v20, a4
	v_accvgpr_read_b32 v21, a5
	v_accvgpr_read_b32 v22, a6
	v_accvgpr_read_b32 v23, a7
	v_accvgpr_read_b32 v24, a8
	v_accvgpr_read_b32 v25, a9
	v_accvgpr_read_b32 v26, a10
	v_accvgpr_read_b32 v27, a11
	v_accvgpr_read_b32 v28, a12
	v_accvgpr_read_b32 v29, a13
	v_accvgpr_read_b32 v30, a14
	v_accvgpr_read_b32 v31, a15
	v_accvgpr_read_b32 v32, a16
	v_accvgpr_read_b32 v33, a17
	v_accvgpr_read_b32 v34, a18
	v_accvgpr_read_b32 v35, a19
	v_accvgpr_read_b32 v36, a20
	v_accvgpr_read_b32 v37, a21
	v_accvgpr_read_b32 v38, a22
	v_accvgpr_read_b32 v39, a23
	v_accvgpr_read_b32 v40, a24
	v_accvgpr_read_b32 v41, a25
	v_accvgpr_read_b32 v42, a26
	v_accvgpr_read_b32 v43, a27
	v_accvgpr_read_b32 v44, a28
	v_accvgpr_read_b32 v45, a29
	v_accvgpr_read_b32 v46, a30
	v_accvgpr_read_b32 v47, a31
	v_add_f32_e32 v16, v14, v16
	v_add_f32_e32 v17, v14, v17
	v_add_f32_e32 v18, v14, v18
	v_add_f32_e32 v19, v14, v19
	v_add_f32_e32 v20, v14, v20
	v_add_f32_e32 v21, v14, v21
	v_add_f32_e32 v22, v14, v22
	v_add_f32_e32 v23, v14, v23
	v_add_f32_e32 v24, v14, v24
	v_add_f32_e32 v25, v14, v25
	v_add_f32_e32 v26, v14, v26
	v_add_f32_e32 v27, v14, v27
	v_add_f32_e32 v28, v14, v28
	v_add_f32_e32 v29, v14, v29
	v_add_f32_e32 v30, v14, v30
	v_add_f32_e32 v31, v14, v31
	v_add_f32_e32 v32, v14, v32
	v_add_f32_e32 v33, v14, v33
	v_add_f32_e32 v34, v14, v34
	v_add_f32_e32 v35, v14, v35
	v_add_f32_e32 v36, v14, v36
	v_add_f32_e32 v37, v14, v37
	v_add_f32_e32 v38, v14, v38
	v_add_f32_e32 v39, v14, v39
	v_add_f32_e32 v40, v14, v40
	v_add_f32_e32 v41, v14, v41
	v_add_f32_e32 v42, v14, v42
	v_add_f32_e32 v43, v14, v43
	v_add_f32_e32 v44, v14, v44
	v_add_f32_e32 v45, v14, v45
	v_add_f32_e32 v46, v14, v46
	v_add_f32_e32 v47, v14, v47
	global_store_dword v15, v16, s[8:9] nt
	s_add_u32 s8, s8, 0x1000
	s_addc_u32 s9, s9, 0
	global_store_dword v15, v17, s[8:9] nt
	s_add_u32 s8, s8, 0x1000
	s_addc_u32 s9, s9, 0
	global_store_dword v15, v18, s[8:9] nt
	s_add_u32 s8, s8, 0x1000
	s_addc_u32 s9, s9, 0
	global_store_dword v15, v19, s[8:9] nt
	s_add_u32 s8, s8, 0x5000
	s_addc_u32 s9, s9, 0
	global_store_dword v15, v20, s[8:9] nt
	s_add_u32 s8, s8, 0x1000
	s_addc_u32 s9, s9, 0
	global_store_dword v15, v21, s[8:9] nt
	s_add_u32 s8, s8, 0x1000
	s_addc_u32 s9, s9, 0
	global_store_dword v15, v22, s[8:9] nt
	s_add_u32 s8, s8, 0x1000
	s_addc_u32 s9, s9, 0
	global_store_dword v15, v23, s[8:9] nt
	s_add_u32 s8, s8, 0x5000
	s_addc_u32 s9, s9, 0
	global_store_dword v15, v24, s[8:9] nt
	s_add_u32 s8, s8, 0x1000
	s_addc_u32 s9, s9, 0
	global_store_dword v15, v25, s[8:9] nt
	s_add_u32 s8, s8, 0x1000
	s_addc_u32 s9, s9, 0
	global_store_dword v15, v26, s[8:9] nt
	s_add_u32 s8, s8, 0x1000
	s_addc_u32 s9, s9, 0
	global_store_dword v15, v27, s[8:9] nt
	s_add_u32 s8, s8, 0x5000
	s_addc_u32 s9, s9, 0
	global_store_dword v15, v28, s[8:9] nt
	s_add_u32 s8, s8, 0x1000
	s_addc_u32 s9, s9, 0
	global_store_dword v15, v29, s[8:9] nt
	s_add_u32 s8, s8, 0x1000
	s_addc_u32 s9, s9, 0
	global_store_dword v15, v30, s[8:9] nt
	s_add_u32 s8, s8, 0x1000
	s_addc_u32 s9, s9, 0
	global_store_dword v15, v31, s[8:9] nt
	s_add_u32 s8, s8, 0x5000
	s_addc_u32 s9, s9, 0
	global_store_dword v15, v32, s[8:9] nt
	s_add_u32 s8, s8, 0x1000
	s_addc_u32 s9, s9, 0
	global_store_dword v15, v33, s[8:9] nt
	s_add_u32 s8, s8, 0x1000
	s_addc_u32 s9, s9, 0
	global_store_dword v15, v34, s[8:9] nt
	s_add_u32 s8, s8, 0x1000
	s_addc_u32 s9, s9, 0
	global_store_dword v15, v35, s[8:9] nt
	s_add_u32 s8, s8, 0x5000
	s_addc_u32 s9, s9, 0
	global_store_dword v15, v36, s[8:9] nt
	s_add_u32 s8, s8, 0x1000
	s_addc_u32 s9, s9, 0
	global_store_dword v15, v37, s[8:9] nt
	s_add_u32 s8, s8, 0x1000
	s_addc_u32 s9, s9, 0
	global_store_dword v15, v38, s[8:9] nt
	s_add_u32 s8, s8, 0x1000
	s_addc_u32 s9, s9, 0
	global_store_dword v15, v39, s[8:9] nt
	s_add_u32 s8, s8, 0x5000
	s_addc_u32 s9, s9, 0
	global_store_dword v15, v40, s[8:9] nt
	s_add_u32 s8, s8, 0x1000
	s_addc_u32 s9, s9, 0
	global_store_dword v15, v41, s[8:9] nt
	s_add_u32 s8, s8, 0x1000
	s_addc_u32 s9, s9, 0
	global_store_dword v15, v42, s[8:9] nt
	s_add_u32 s8, s8, 0x1000
	s_addc_u32 s9, s9, 0
	global_store_dword v15, v43, s[8:9] nt
	s_add_u32 s8, s8, 0x5000
	s_addc_u32 s9, s9, 0
	global_store_dword v15, v44, s[8:9] nt
	s_add_u32 s8, s8, 0x1000
	s_addc_u32 s9, s9, 0
	global_store_dword v15, v45, s[8:9] nt
	s_add_u32 s8, s8, 0x1000
	s_addc_u32 s9, s9, 0
	global_store_dword v15, v46, s[8:9] nt
	s_add_u32 s8, s8, 0x1000
	s_addc_u32 s9, s9, 0
	global_store_dword v15, v47, s[8:9] nt
	s_endpgm

	.amdhsa_kernel _Z11gemm_kernelILi1ELi1EEvPKDF16_S1_iiPKfS3_S3_PDF16_S4_S4_Pf
		.amdhsa_group_segment_fixed_size 73728
		.amdhsa_private_segment_fixed_size 0
		.amdhsa_kernarg_size 336
		.amdhsa_user_sgpr_count 2
		.amdhsa_user_sgpr_dispatch_ptr 0
		.amdhsa_user_sgpr_queue_ptr 0
		.amdhsa_user_sgpr_kernarg_segment_ptr 1
		.amdhsa_user_sgpr_dispatch_id 0
		.amdhsa_user_sgpr_kernarg_preload_length 0
		.amdhsa_user_sgpr_kernarg_preload_offset 0
		.amdhsa_user_sgpr_private_segment_size 0
		.amdhsa_uses_dynamic_stack 0
		.amdhsa_enable_private_segment 0
		.amdhsa_system_sgpr_workgroup_id_x 1
		.amdhsa_system_sgpr_workgroup_id_y 0
		.amdhsa_system_sgpr_workgroup_id_z 0
		.amdhsa_system_sgpr_workgroup_info 0
		.amdhsa_system_vgpr_workitem_id 0
		.amdhsa_next_free_vgpr 96
		.amdhsa_next_free_sgpr 32
		.amdhsa_accum_offset 64
		.amdhsa_reserve_vcc 0
		.amdhsa_float_round_mode_32 0
		.amdhsa_float_round_mode_16_64 0
		.amdhsa_float_denorm_mode_32 3
		.amdhsa_float_denorm_mode_16_64 3
		.amdhsa_dx10_clamp 1
		.amdhsa_ieee_mode 1
		.amdhsa_fp16_overflow 0
		.amdhsa_tg_split 0
		.amdhsa_exception_fp_ieee_invalid_op 0
		.amdhsa_exception_fp_denorm_src 0
		.amdhsa_exception_fp_ieee_div_zero 0
		.amdhsa_exception_fp_ieee_overflow 0
		.amdhsa_exception_fp_ieee_underflow 0
		.amdhsa_exception_fp_ieee_inexact 0
		.amdhsa_exception_int_div_zero 0
	.end_amdhsa_kernel

amdhsa.kernels:
  - .agpr_count:     0
    .args:
      - .actual_access:  read_only
        .address_space:  global
        .offset:         0
        .size:           8
        .value_kind:     global_buffer
      - .actual_access:  read_only
        .address_space:  global
        .offset:         8
        .size:           8
        .value_kind:     global_buffer
      - .actual_access:  read_only
        .address_space:  global
        .offset:         16
        .size:           8
        .value_kind:     global_buffer
      - .actual_access:  read_only
        .address_space:  global
        .offset:         24
        .size:           8
        .value_kind:     global_buffer
      - .actual_access:  read_only
        .address_space:  global
        .offset:         32
        .size:           8
        .value_kind:     global_buffer
      - .actual_access:  read_only
        .address_space:  global
        .offset:         40
        .size:           8
        .value_kind:     global_buffer
      - .actual_access:  write_only
        .address_space:  global
        .offset:         48
        .size:           8
        .value_kind:     global_buffer
      - .actual_access:  write_only
        .address_space:  global
        .offset:         56
        .size:           8
        .value_kind:     global_buffer
      - .actual_access:  write_only
        .address_space:  global
        .offset:         64
        .size:           8
        .value_kind:     global_buffer
    .group_segment_fixed_size: 9216
    .kernarg_segment_align: 8
    .kernarg_segment_size: 72
    .language:       OpenCL C
    .language_version:
      - 2
      - 0
    .max_flat_workgroup_size: 256
    .name:           _Z11prep_kernelPKfS0_S0_S0_S0_S0_PDF16_S1_S1_
    .private_segment_fixed_size: 0
    .sgpr_count:     22
    .sgpr_spill_count: 0
    .symbol:         _Z11prep_kernelPKfS0_S0_S0_S0_S0_PDF16_S1_S1_.kd
    .uniform_work_group_size: 1
    .uses_dynamic_stack: false
    .vgpr_count:     38
    .vgpr_spill_count: 0
    .wavefront_size: 64
  - .agpr_count:     0
    .args:
      - .address_space:  global
        .offset:         0
        .size:           8
        .value_kind:     global_buffer
      - .address_space:  global
        .offset:         8
        .size:           8
        .value_kind:     global_buffer
      - .actual_access:  read_only
        .address_space:  global
        .offset:         16
        .size:           8
        .value_kind:     global_buffer
      - .actual_access:  read_only
        .address_space:  global
        .offset:         24
        .size:           8
        .value_kind:     global_buffer
      - .actual_access:  read_only
        .address_space:  global
        .offset:         32
        .size:           8
        .value_kind:     global_buffer
      - .actual_access:  write_only
        .address_space:  global
        .offset:         40
        .size:           8
        .value_kind:     global_buffer
      - .actual_access:  write_only
        .address_space:  global
        .offset:         48
        .size:           8
        .value_kind:     global_buffer
      - .actual_access:  write_only
        .address_space:  global
        .offset:         56
        .size:           8
        .value_kind:     global_buffer
    .group_segment_fixed_size: 118784
    .kernarg_segment_align: 8
    .kernarg_segment_size: 64
    .language:       OpenCL C
    .language_version:
      - 2
      - 0
    .max_flat_workgroup_size: 512
    .name:           _Z15qkv_gemm_kernelPKDF16_S0_PKfS2_S2_PDF16_S3_S3_
    .private_segment_fixed_size: 0
    .sgpr_count:     49
    .sgpr_spill_count: 0
    .symbol:         _Z15qkv_gemm_kernelPKDF16_S0_PKfS2_S2_PDF16_S3_S3_.kd
    .uniform_work_group_size: 1
    .uses_dynamic_stack: false
    .vgpr_count:     212
    .vgpr_spill_count: 0
    .wavefront_size: 64
  - .agpr_count:     0
    .args:
      - .actual_access:  read_only
        .address_space:  global
        .offset:         0
        .size:           8
        .value_kind:     global_buffer
      - .address_space:  global
        .offset:         8
        .size:           8
        .value_kind:     global_buffer
      - .address_space:  global
        .offset:         16
        .size:           8
        .value_kind:     global_buffer
      - .address_space:  global
        .offset:         24
        .size:           8
        .value_kind:     global_buffer
      - .actual_access:  write_only
        .address_space:  global
        .offset:         32
        .size:           8
        .value_kind:     global_buffer
    .group_segment_fixed_size: 163840
    .kernarg_segment_align: 8
    .kernarg_segment_size: 40
    .language:       OpenCL C
    .language_version:
      - 2
      - 0
    .max_flat_workgroup_size: 512
    .name:           _Z11attn_kernelPKDF16_S0_S0_S0_PDF16_
    .private_segment_fixed_size: 0
    .sgpr_count:     106
    .sgpr_spill_count: 42
    .symbol:         _Z11attn_kernelPKDF16_S0_S0_S0_PDF16_.kd
    .uniform_work_group_size: 1
    .uses_dynamic_stack: false
    .vgpr_count:     253
    .vgpr_spill_count: 0
    .wavefront_size: 64
  - .agpr_count:     32
    .args:
      - .address_space:  global
        .offset:         0
        .size:           8
        .value_kind:     global_buffer
      - .address_space:  global
        .offset:         8
        .size:           8
        .value_kind:     global_buffer
      - .offset:         16
        .size:           4
        .value_kind:     by_value
      - .offset:         20
        .size:           4
        .value_kind:     by_value
      - .actual_access:  read_only
        .address_space:  global
        .offset:         24
        .size:           8
        .value_kind:     global_buffer
      - .actual_access:  read_only
        .address_space:  global
        .offset:         32
        .size:           8
        .value_kind:     global_buffer
      - .actual_access:  read_only
        .address_space:  global
        .offset:         40
        .size:           8
        .value_kind:     global_buffer
      - .actual_access:  read_only
        .address_space:  global
        .offset:         48
        .size:           8
        .value_kind:     global_buffer
      - .actual_access:  read_only
        .address_space:  global
        .offset:         56
        .size:           8
        .value_kind:     global_buffer
      - .actual_access:  read_only
        .address_space:  global
        .offset:         64
        .size:           8
        .value_kind:     global_buffer
      - .actual_access:  write_only
        .address_space:  global
        .offset:         72
        .size:           8
        .value_kind:     global_buffer
      - .offset:         80
        .size:           4
        .value_kind:     hidden_block_count_x
      - .offset:         84
        .size:           4
        .value_kind:     hidden_block_count_y
      - .offset:         88
        .size:           4
        .value_kind:     hidden_block_count_z
      - .offset:         92
        .size:           2
        .value_kind:     hidden_group_size_x
      - .offset:         94
        .size:           2
        .value_kind:     hidden_group_size_y
      - .offset:         96
        .size:           2
        .value_kind:     hidden_group_size_z
      - .offset:         98
        .size:           2
        .value_kind:     hidden_remainder_x
      - .offset:         100
        .size:           2
        .value_kind:     hidden_remainder_y
      - .offset:         102
        .size:           2
        .value_kind:     hidden_remainder_z
      - .offset:         120
        .size:           8
        .value_kind:     hidden_global_offset_x
      - .offset:         128
        .size:           8
        .value_kind:     hidden_global_offset_y
      - .offset:         136
        .size:           8
        .value_kind:     hidden_global_offset_z
      - .offset:         144
        .size:           2
        .value_kind:     hidden_grid_dims
    .group_segment_fixed_size: 73728
    .kernarg_segment_align: 8
    .kernarg_segment_size: 336
    .language:       OpenCL C
    .language_version:
      - 2
      - 0
    .max_flat_workgroup_size: 256
    .name:           _Z11gemm_kernelILi1ELi1EEvPKDF16_S1_iiPKfS3_S3_PDF16_S4_S4_Pf
    .private_segment_fixed_size: 0
    .sgpr_count:     38
    .sgpr_spill_count: 0
    .symbol:         _Z11gemm_kernelILi1ELi1EEvPKDF16_S1_iiPKfS3_S3_PDF16_S4_S4_Pf.kd
    .uniform_work_group_size: 1
    .uses_dynamic_stack: false
    .vgpr_count:     96
    .vgpr_spill_count: 0
    .wavefront_size: 64
